# v44 + norm phases 6 and 9: next row's H pieces loaded one row ahead (two rows in flight per wave)
# speedup vs baseline: 1.0130x; 1.0130x over previous
; #define GAS __attribute__((address_space(1)))
; template <bool F8, bool SRCH = false> __device__ __forceinline__ void norm_phase(Frame& F, const float* srcL, const float* srcC, const float* g, const float* mod, int shift_off, int scale_off, int nrows) {
;     const int gw = F.vcu * NWAVES + F.wave, NGW = F.G * NWAVES;
;     bf16* XN = WSP(bf16, WS_XN);
;     for (int row = gw; row < nrows; row += NGW) {
;         const float* src = row < ML ? srcL + (size_t)row * DM : srcC + (size_t)(row - ML) * DM;
;         const float* mv = mod + (size_t)(row < ML ? (row >> 13) : 2) * MOD_W;
;         const GAS f32x4* xr = (const GAS f32x4*)src + F.lane;
;         f32x4 v[8]; float s = 0.f;
; #pragma unroll
;         for (int j = 0; j < 8; ++j) {
;             if constexpr (SRCH) { const v2u w = ((const GAS v2u*)(WSP(const bf16, WS_H) + (size_t)row * DM))[F.lane + 64 * j]; v[j].x = bflo(w.x); v[j].y = bfhi(w.x); v[j].z = bflo(w.y); v[j].w = bfhi(w.y); }
;             else v[j] = xr[64 * j];
;             s += (v[j].x * v[j].x + v[j].y * v[j].y) + (v[j].z * v[j].z + v[j].w * v[j].w); }
;         const float rstd = 1.0f / sqrtf(wave_sum(s) * (1.0f / DM) + NORM_EPS);
;         GAS v2u* o8 = (GAS v2u*)(XN + (size_t)row * DM) + F.lane;
; #pragma unroll
;         for (int j = 0; j < 8; ++j) { const int col = 4 * (F.lane + 64 * j);
;             const f32x4 gg = *(const GAS f32x4*)(g + col), sh = *(const GAS f32x4*)(mv + shift_off + col), sc = *(const GAS f32x4*)(mv + scale_off + col);
.LBB0_600:
	s_cmp_lt_i32 s90, 7
	s_cselect_b64 s[2:3], -1, 0
	s_and_b64 s[2:3], s[2:3], s[0:1]
	s_andn2_b64 vcc, exec, s[2:3]
	s_cbranch_vccnz .LBB0_604
	s_lshl_b32 s0, s92, 3
	s_add_i32 s4, s0, s94
	s_cmpk_gt_i32 s4, 0x41ff
	s_cbranch_scc1 .LBB0_604
	v_mbcnt_lo_u32_b32 v1, -1, 0
	s_waitcnt vmcnt(0)
	v_mbcnt_hi_u32_b32 v2, -1, v1
	v_and_b32_e32 v1, 64, v2
	v_add_u32_e32 v3, 64, v1
	v_xor_b32_e32 v1, 1, v2
	v_cmp_lt_i32_e32 vcc, v1, v3
	v_xor_b32_e32 v4, 2, v2
	v_readlane_b32 s52, v250, 24
	v_cndmask_b32_e32 v1, v2, v1, vcc
	v_cmp_lt_i32_e32 vcc, v4, v3
	v_readlane_b32 s60, v250, 32
	v_readlane_b32 s61, v250, 33
	v_cndmask_b32_e32 v4, v2, v4, vcc
	v_lshlrev_b32_e32 v42, 2, v4
	v_xor_b32_e32 v4, 4, v2
	v_cmp_lt_i32_e32 vcc, v4, v3
	v_mov_b32_e32 v17, 0
	v_lshlrev_b32_e32 v16, 4, v178
	v_cndmask_b32_e32 v4, v2, v4, vcc
	v_lshlrev_b32_e32 v43, 2, v4
	v_xor_b32_e32 v4, 8, v2
	v_cmp_lt_i32_e32 vcc, v4, v3
	s_mov_b64 s[8:9], s[60:61]
	v_or_b32_e32 v6, 0x80, v178
	v_cndmask_b32_e32 v4, v2, v4, vcc
	v_lshlrev_b32_e32 v44, 2, v4
	v_xor_b32_e32 v4, 16, v2
	v_cmp_lt_i32_e32 vcc, v4, v3
	v_or_b32_e32 v8, 0xc0, v178
	v_lshlrev_b32_e32 v26, 2, v6
	v_cndmask_b32_e32 v4, v2, v4, vcc
	v_lshlrev_b32_e32 v45, 2, v4
	v_xor_b32_e32 v4, 32, v2
	v_cmp_lt_i32_e32 vcc, v4, v3
	v_or_b32_e32 v10, 0x100, v178
	v_lshlrev_b32_e32 v28, 2, v8
	v_cndmask_b32_e32 v2, v2, v4, vcc
	v_or_b32_e32 v4, 64, v178
	v_lshlrev_b32_e32 v46, 2, v2
	v_lshl_add_u64 v[2:3], s[8:9], 0, v[16:17]
	v_lshlrev_b32_e32 v16, 4, v4
	v_lshlrev_b32_e32 v24, 2, v4
	v_lshl_add_u64 v[4:5], s[8:9], 0, v[16:17]
	v_lshlrev_b32_e32 v16, 4, v6
	v_lshl_add_u64 v[6:7], s[8:9], 0, v[16:17]
	v_lshlrev_b32_e32 v16, 4, v8
	v_lshl_add_u64 v[8:9], s[8:9], 0, v[16:17]
	v_lshlrev_b32_e32 v16, 4, v10
	v_or_b32_e32 v12, 0x140, v178
	s_add_u32 s16, s88, 0x100000
	v_lshlrev_b32_e32 v30, 2, v10
	v_lshl_add_u64 v[10:11], s[8:9], 0, v[16:17]
	v_lshlrev_b32_e32 v16, 4, v12
	v_or_b32_e32 v14, 0x180, v178
	s_addc_u32 s17, s89, 0
	v_lshlrev_b32_e32 v32, 2, v12
	v_lshl_add_u64 v[12:13], s[8:9], 0, v[16:17]
	v_lshlrev_b32_e32 v16, 4, v14
	s_ashr_i32 s5, s4, 31
	s_lshl_b32 s6, s93, 3
	v_lshlrev_b32_e32 v22, 2, v178
	v_lshlrev_b32_e32 v34, 2, v14
	v_lshl_add_u64 v[14:15], s[8:9], 0, v[16:17]
	v_or_b32_e32 v16, 0x1c0, v178
	s_lshl_b64 s[0:1], s[4:5], 11
	v_lshlrev_b32_e32 v36, 2, v16
	v_lshlrev_b32_e32 v16, 4, v16
	v_or_b32_e32 v18, s0, v22
	v_mov_b32_e32 v19, s1
	s_ashr_i32 s7, s6, 31
	s_lshl_b64 s[0:1], s[4:5], 12
	v_lshlrev_b32_e32 v1, 2, v1
	v_lshl_add_u64 v[16:17], s[8:9], 0, v[16:17]
	s_lshl_b64 s[8:9], s[6:7], 11
	v_lshl_or_b32 v20, v178, 3, s0
	v_mov_b32_e32 v21, s1
	s_lshl_b64 s[10:11], s[6:7], 12
	v_mov_b32_e32 v47, 0x358637bd
	s_mov_b32 s5, 0xf800000
	v_mov_b32_e32 v48, 0x260
	v_lshlrev_b32_e32 v49, 2, v22
	s_mov_b32 s7, 0xc3e00000
	s_mov_b32 s18, 0x1da00000
	v_lshlrev_b32_e32 v50, 2, v24
	v_lshlrev_b32_e32 v51, 2, v26
	v_lshlrev_b32_e32 v52, 2, v28
	v_lshlrev_b32_e32 v53, 2, v30
	v_lshlrev_b32_e32 v54, 2, v32
	v_lshlrev_b32_e32 v55, 2, v34
	v_lshlrev_b32_e32 v56, 2, v36
	v_mov_b32_e32 v57, 0x43e00000
	v_readlane_b32 s53, v250, 25
	v_readlane_b32 s54, v250, 26
	v_readlane_b32 s55, v250, 27
	v_readlane_b32 s56, v250, 28
	v_readlane_b32 s57, v250, 29
	v_readlane_b32 s58, v250, 30
	v_readlane_b32 s59, v250, 31
	v_readlane_b32 s62, v250, 34
	v_readlane_b32 s63, v250, 35
	v_readlane_b32 s64, v250, 36
	v_readlane_b32 s65, v250, 37
	v_readlane_b32 s66, v250, 38
	v_readlane_b32 s67, v250, 39
	v_lshl_add_u64 v[24:25], s[88:89], 0, v[20:21]
	v_add_co_u32_e32 v24, vcc, 0x4d800000, v24
	s_nop 0
	v_addc_co_u32_e32 v25, vcc, 0, v25, vcc
	global_load_dwordx2 v[26:27], v[24:25], off
	global_load_dwordx2 v[28:29], v[24:25], off offset:512
	global_load_dwordx2 v[30:31], v[24:25], off offset:1024
	global_load_dwordx2 v[32:33], v[24:25], off offset:1536
	global_load_dwordx2 v[34:35], v[24:25], off offset:2048
	global_load_dwordx2 v[36:37], v[24:25], off offset:2560
	global_load_dwordx2 v[70:71], v[24:25], off offset:3072
	global_load_dwordx2 v[72:73], v[24:25], off offset:3584
.LBB0_603:
	v_lshl_add_u64 v[24:25], s[88:89], 0, v[20:21]
	v_add_co_u32_e32 v24, vcc, 0x4d800000, v24
	global_load_dwordx4 v[58:61], v[2:3], off
	s_nop 0
	v_addc_co_u32_e32 v25, vcc, 0, v25, vcc
	s_min_i32 s0, s4, 0x4000
	v_lshl_add_u64 v[22:23], s[88:89], 0, v[18:19]
	s_ashr_i32 s12, s0, 13
	v_add_co_u32_e64 v22, s[0:1], s18, v22
	v_mov_b32_e32 v110, 0
	s_nop 0
	v_addc_co_u32_e64 v23, s[0:1], 0, v23, s[0:1]
	s_mul_hi_i32 s0, s12, 0xc000
	s_mul_i32 s12, s12, 0xc000
	s_add_u32 s1, s16, s12
	s_addc_u32 s0, s17, s0
	s_add_u32 s12, s1, 0x6000
	s_addc_u32 s13, s0, 0
	s_add_u32 s14, s1, 0x8000
	s_addc_u32 s15, s0, 0
	global_load_dwordx4 v[62:65], v49, s[12:13]
	global_load_dwordx4 v[66:69], v49, s[14:15]
	global_load_dwordx4 v[118:121], v[4:5], off
	global_load_dwordx4 v[122:125], v50, s[14:15]
	global_load_dwordx4 v[126:129], v50, s[12:13]
	global_load_dwordx4 v[130:133], v[6:7], off
	global_load_dwordx4 v[134:137], v51, s[14:15]
	global_load_dwordx4 v[138:141], v51, s[12:13]
	global_load_dwordx4 v[142:145], v[8:9], off
	global_load_dwordx4 v[146:149], v52, s[14:15]
	global_load_dwordx4 v[150:153], v52, s[12:13]
	global_load_dwordx4 v[154:157], v[10:11], off
	global_load_dwordx4 v[158:161], v53, s[14:15]
	global_load_dwordx4 v[162:165], v53, s[12:13]
	global_load_dwordx4 v[166:169], v[12:13], off
	global_load_dwordx4 v[170:173], v54, s[14:15]
	global_load_dwordx4 v[174:177], v54, s[12:13]
	global_load_dwordx4 v[182:185], v[14:15], off
	global_load_dwordx4 v[186:189], v55, s[14:15]
	global_load_dwordx4 v[190:193], v55, s[12:13]
	global_load_dwordx4 v[194:197], v[16:17], off
	global_load_dwordx4 v[198:201], v56, s[14:15]
	global_load_dwordx4 v[202:205], v56, s[12:13]
	s_add_i32 s4, s4, s6
	v_lshl_add_u64 v[18:19], v[18:19], 0, s[8:9]
	v_lshl_add_u64 v[20:21], v[20:21], 0, s[10:11]
	s_cmpk_lt_i32 s4, 0x4200
	v_lshl_add_u64 v[222:223], v[24:25], 0, s[10:11]
	global_load_dwordx2 v[206:207], v[222:223], off
	global_load_dwordx2 v[208:209], v[222:223], off offset:512
	global_load_dwordx2 v[210:211], v[222:223], off offset:1024
	global_load_dwordx2 v[212:213], v[222:223], off offset:1536
	global_load_dwordx2 v[214:215], v[222:223], off offset:2048
	global_load_dwordx2 v[216:217], v[222:223], off offset:2560
	global_load_dwordx2 v[218:219], v[222:223], off offset:3072
	global_load_dwordx2 v[220:221], v[222:223], off offset:3584
	s_waitcnt vmcnt(32)
; #define GAS __attribute__((address_space(1)))
; __device__ __forceinline__ unsigned pk4_fp8(float a, float b, float c, float d) { int p = 0; p = __builtin_amdgcn_cvt_pk_fp8_f32(a, b, p, false); p = __builtin_amdgcn_cvt_pk_fp8_f32(c, d, p, true); return (unsigned)p; }
; __device__ __forceinline__ float clamp8(float x) { return __builtin_fminf(__builtin_fmaxf(x, -448.0f), 448.0f); }
; template <bool F8, bool SRCH = false> __device__ __forceinline__ void norm_phase(Frame& F, const float* srcL, const float* srcC, const float* g, const float* mod, int shift_off, int scale_off, int nrows) {
;     ...
;             s += (v[j].x * v[j].x + v[j].y * v[j].y) + (v[j].z * v[j].z + v[j].w * v[j].w); }
;         const float rstd = 1.0f / sqrtf(wave_sum(s) * (1.0f / DM) + NORM_EPS);
;         GAS v2u* o8 = (GAS v2u*)(XN + (size_t)row * DM) + F.lane;
; #pragma unroll
;         for (int j = 0; j < 8; ++j) { const int col = 4 * (F.lane + 64 * j);
;             const f32x4 gg = *(const GAS f32x4*)(g + col), sh = *(const GAS f32x4*)(mv + shift_off + col), sc = *(const GAS f32x4*)(mv + scale_off + col);
;             const f32x4 y = v[j] * rstd * gg * (sc + 1.0f) + sh;
;             if (F8) { ((GAS unsigned*)((unsigned char*)XN + (size_t)row * DM))[F.lane + 64 * j] = pk4_fp8(clamp8(y.x), clamp8(y.y), clamp8(y.z), clamp8(y.w)); }
	v_and_b32_e32 v75, 0xffff0000, v26
	v_and_b32_e32 v77, 0xffff0000, v27
	v_lshlrev_b32_e32 v74, 16, v26
	v_lshlrev_b32_e32 v76, 16, v27
	v_and_b32_e32 v81, 0xffff0000, v29
	v_and_b32_e32 v80, 0xffff0000, v28
	v_and_b32_e32 v83, 0xffff0000, v30
	v_and_b32_e32 v85, 0xffff0000, v31
	v_lshlrev_b32_e32 v87, 16, v32
	v_lshlrev_b32_e32 v27, 16, v72
	v_and_b32_e32 v25, 0xffff0000, v72
	v_mul_f32_e32 v24, v77, v77
	v_mul_f32_e32 v26, v75, v75
	v_lshlrev_b32_e32 v79, 16, v29
	v_lshlrev_b32_e32 v78, 16, v28
	v_lshlrev_b32_e32 v82, 16, v30
	v_lshlrev_b32_e32 v84, 16, v31
	v_and_b32_e32 v89, 0xffff0000, v32
	v_lshlrev_b32_e32 v90, 16, v33
	v_and_b32_e32 v91, 0xffff0000, v33
	v_lshlrev_b32_e32 v30, 16, v70
	v_and_b32_e32 v31, 0xffff0000, v70
	v_lshlrev_b32_e32 v32, 16, v71
	v_and_b32_e32 v33, 0xffff0000, v71
	v_lshlrev_b32_e32 v28, 16, v73
	v_and_b32_e32 v29, 0xffff0000, v73
	v_pk_mul_f32 v[70:71], v[80:81], v[80:81]
	v_mov_b32_e32 v73, v87
	v_mul_f32_e32 v72, v83, v83
	v_mul_f32_e32 v86, v85, v85
	v_pk_fma_f32 v[98:99], v[76:77], v[76:77], v[24:25] op_sel_hi:[1,1,0]
	v_pk_fma_f32 v[100:101], v[74:75], v[74:75], v[26:27] op_sel_hi:[1,1,0]
	v_pk_fma_f32 v[70:71], v[78:79], v[78:79], v[70:71]
	v_pk_fma_f32 v[102:103], v[82:83], v[82:83], v[72:73] op_sel_hi:[1,1,0]
	v_pk_fma_f32 v[104:105], v[84:85], v[84:85], v[86:87] op_sel_hi:[1,1,0]
	v_mov_b32_e32 v86, v100
	v_mov_b32_e32 v72, v98
	v_mul_f32_e32 v111, v89, v89
	v_mul_f32_e32 v112, v90, v90
	v_mul_f32_e32 v113, v91, v91
	v_pk_add_f32 v[98:99], v[100:101], v[98:99]
	v_pk_add_f32 v[70:71], v[70:71], v[70:71] op_sel:[0,1] op_sel_hi:[1,0]
	v_pk_mul_f32 v[72:73], v[86:87], v[72:73]
	v_and_b32_e32 v41, 0xffff0000, v35
	v_and_b32_e32 v40, 0xffff0000, v34
	v_mov_b32_e32 v103, v112
	v_mov_b32_e32 v105, v113
	v_mov_b32_e32 v71, v111
	v_mov_b32_e32 v99, v73
	v_lshlrev_b32_e32 v39, 16, v35
	v_lshlrev_b32_e32 v38, 16, v34
	v_pk_mul_f32 v[92:93], v[40:41], v[40:41]
	v_pk_add_f32 v[100:101], v[102:103], v[104:105]
	v_pk_add_f32 v[70:71], v[98:99], v[70:71]
	v_lshlrev_b32_e32 v35, 16, v37
	v_lshlrev_b32_e32 v34, 16, v36
	v_and_b32_e32 v37, 0xffff0000, v37
	v_and_b32_e32 v36, 0xffff0000, v36
	v_pk_fma_f32 v[92:93], v[38:39], v[38:39], v[92:93]
	v_pk_add_f32 v[70:71], v[70:71], v[100:101]
	v_pk_mul_f32 v[94:95], v[36:37], v[36:37]
	v_mov_b32_e32 v97, v27
	v_mul_f32_e32 v96, v33, v33
	v_pk_add_f32 v[92:93], v[92:93], v[92:93] op_sel:[0,1] op_sel_hi:[1,0]
	v_pk_add_f32 v[70:71], v[70:71], v[70:71] op_sel:[0,1] op_sel_hi:[1,0]
	v_mul_f32_e32 v88, v31, v31
	v_pk_fma_f32 v[94:95], v[34:35], v[34:35], v[94:95]
	v_pk_fma_f32 v[108:109], v[32:33], v[32:33], v[96:97] op_sel_hi:[1,1,0]
	v_mov_b32_e32 v96, v92
	v_mov_b32_e32 v26, v70
	v_mul_f32_e32 v114, v25, v25
	v_mul_f32_e32 v115, v28, v28
	v_mul_f32_e32 v116, v29, v29
	v_pk_fma_f32 v[106:107], v[30:31], v[30:31], v[88:89] op_sel_hi:[1,1,0]
	v_pk_add_f32 v[94:95], v[94:95], v[94:95] op_sel:[0,1] op_sel_hi:[1,0]
	v_pk_add_f32 v[70:71], v[70:71], v[92:93]
	v_pk_mul_f32 v[72:73], v[26:27], v[96:97]
	v_mov_b32_e32 v107, v115
	v_mov_b32_e32 v109, v116
	v_mov_b32_e32 v95, v114
	v_mov_b32_e32 v71, v73
	v_pk_add_f32 v[102:103], v[106:107], v[108:109]
	v_pk_add_f32 v[70:71], v[70:71], v[94:95]
	s_waitcnt vmcnt(8)
	v_pk_add_f32 v[66:67], v[66:67], 1.0 op_sel_hi:[1,0]
	v_pk_add_f32 v[70:71], v[70:71], v[102:103]
	v_pk_add_f32 v[68:69], v[68:69], 1.0 op_sel_hi:[1,0]
	v_add_f32_e32 v24, v70, v71
	ds_bpermute_b32 v26, v1, v24
	v_mov_b32_e32 v88, v87
	s_waitcnt lgkmcnt(0)
	v_add_f32_e32 v24, v24, v26
	ds_bpermute_b32 v26, v42, v24
	s_waitcnt lgkmcnt(0)
	v_add_f32_e32 v24, v24, v26
	ds_bpermute_b32 v26, v43, v24
	s_waitcnt lgkmcnt(0)
	v_add_f32_e32 v24, v24, v26
	ds_bpermute_b32 v26, v44, v24
	s_waitcnt lgkmcnt(0)
	v_add_f32_e32 v24, v24, v26
	ds_bpermute_b32 v26, v45, v24
	s_waitcnt lgkmcnt(0)
	v_add_f32_e32 v24, v24, v26
	ds_bpermute_b32 v26, v46, v24
	s_waitcnt lgkmcnt(0)
	v_add_f32_e32 v24, v24, v26
	v_fmamk_f32 v24, v24, 0x3a000000, v47
	v_mul_f32_e32 v26, 0x4f800000, v24
	v_cmp_gt_f32_e32 vcc, s5, v24
	s_nop 1
	v_cndmask_b32_e32 v24, v24, v26, vcc
	v_sqrt_f32_e32 v26, v24
	s_nop 0
	v_add_u32_e32 v70, -1, v26
	v_add_u32_e32 v71, 1, v26
	v_fma_f32 v72, -v70, v26, v24
	v_fma_f32 v73, -v71, v26, v24
	v_cmp_ge_f32_e64 s[0:1], 0, v72
	s_nop 1
	v_cndmask_b32_e64 v26, v26, v70, s[0:1]
	v_cmp_lt_f32_e64 s[0:1], 0, v73
	s_nop 1
	v_cndmask_b32_e64 v26, v26, v71, s[0:1]
	v_mul_f32_e32 v70, 0x37800000, v26
	v_cndmask_b32_e32 v26, v26, v70, vcc
	v_cmp_class_f32_e32 vcc, v24, v48
	s_nop 1
	v_cndmask_b32_e32 v24, v26, v24, vcc
	v_div_scale_f32 v26, s[0:1], v24, v24, 1.0
	v_rcp_f32_e32 v71, v26
	v_div_scale_f32 v70, vcc, 1.0, v24, 1.0
	v_fma_f32 v72, -v26, v71, 1.0
	v_fmac_f32_e32 v71, v72, v71
	v_mul_f32_e32 v72, v70, v71
	v_fma_f32 v73, -v26, v72, v70
	v_fmac_f32_e32 v72, v73, v71
	v_fma_f32 v26, -v26, v72, v70
	v_div_fmas_f32 v26, v26, v71, v72
	v_div_fixup_f32 v26, v26, v24, 1.0
	v_pk_mul_f32 v[72:73], v[26:27], v[74:75] op_sel_hi:[0,1]
	v_pk_mul_f32 v[58:59], v[58:59], v[72:73]
	v_pk_mul_f32 v[70:71], v[26:27], v[76:77] op_sel_hi:[0,1]
	v_pk_fma_f32 v[58:59], v[66:67], v[58:59], v[62:63]
	v_pk_mul_f32 v[60:61], v[60:61], v[70:71]
	v_med3_f32 v24, v58, s7, v57
	v_med3_f32 v58, v59, s7, v57
	v_cvt_pk_fp8_f32 v110, v24, v58
	v_pk_fma_f32 v[60:61], v[68:69], v[60:61], v[64:65]
	v_mov_b32_e32 v70, v79
	v_med3_f32 v59, v60, s7, v57
	v_med3_f32 v60, v61, s7, v57
	v_cvt_pk_fp8_f32 v110, v59, v60 op_sel:[0,0,1]
	v_mov_b32_e32 v79, v80
	v_pk_mul_f32 v[72:73], v[26:27], v[78:79] op_sel_hi:[0,1]
	v_mov_b32_e32 v24, 0
	global_store_dword v[22:23], v110, off
	v_mov_b32_e32 v58, v118
	v_mov_b32_e32 v59, v119
; #define GAS __attribute__((address_space(1)))
; __device__ __forceinline__ unsigned pk2(float lo, float hi) { return pg8::cvt_pk_bf16(lo, hi); }
; __device__ __forceinline__ unsigned pk4_fp8(float a, float b, float c, float d) { int p = 0; p = __builtin_amdgcn_cvt_pk_fp8_f32(a, b, p, false); p = __builtin_amdgcn_cvt_pk_fp8_f32(c, d, p, true); return (unsigned)p; }
; __device__ __forceinline__ float clamp8(float x) { return __builtin_fminf(__builtin_fmaxf(x, -448.0f), 448.0f); }
; template <bool F8, bool SRCH = false> __device__ __forceinline__ void norm_phase(Frame& F, const float* srcL, const float* srcC, const float* g, const float* mod, int shift_off, int scale_off, int nrows) {
;     ...
;         for (int j = 0; j < 8; ++j) { const int col = 4 * (F.lane + 64 * j);
;             const f32x4 gg = *(const GAS f32x4*)(g + col), sh = *(const GAS f32x4*)(mv + shift_off + col), sc = *(const GAS f32x4*)(mv + scale_off + col);
;             const f32x4 y = v[j] * rstd * gg * (sc + 1.0f) + sh;
;             if (F8) { ((GAS unsigned*)((unsigned char*)XN + (size_t)row * DM))[F.lane + 64 * j] = pk4_fp8(clamp8(y.x), clamp8(y.y), clamp8(y.z), clamp8(y.w)); }
;             else { v2u w; w.x = pk2(y.x, y.y); w.y = pk2(y.z, y.w); o8[64 * j] = w; } }
	v_mov_b32_e32 v60, v120
	v_mov_b32_e32 v61, v121
	v_mov_b32_e32 v62, v122
	v_mov_b32_e32 v63, v123
	v_mov_b32_e32 v64, v124
	v_mov_b32_e32 v65, v125
	v_mov_b32_e32 v66, v126
	v_mov_b32_e32 v67, v127
	v_mov_b32_e32 v68, v128
	v_mov_b32_e32 v69, v129
	v_mov_b32_e32 v71, v81
	v_pk_mul_f32 v[70:71], v[26:27], v[70:71] op_sel_hi:[0,1]
	v_pk_mul_f32 v[32:33], v[26:27], v[32:33] op_sel_hi:[0,1]
	v_pk_mul_f32 v[30:31], v[26:27], v[30:31] op_sel_hi:[0,1]
	v_pk_mul_f32 v[28:29], v[28:29], v[26:27] op_sel_hi:[1,0]
	v_pk_mul_f32 v[58:59], v[58:59], v[72:73]
	v_pk_add_f32 v[62:63], v[62:63], 1.0 op_sel_hi:[1,0]
	v_pk_mul_f32 v[60:61], v[60:61], v[70:71]
	v_pk_fma_f32 v[58:59], v[62:63], v[58:59], v[66:67]
	v_pk_add_f32 v[64:65], v[64:65], 1.0 op_sel_hi:[1,0]
	v_med3_f32 v58, v58, s7, v57
	v_med3_f32 v59, v59, s7, v57
	v_cvt_pk_fp8_f32 v24, v58, v59
	v_pk_fma_f32 v[60:61], v[64:65], v[60:61], v[68:69]
	v_pk_mul_f32 v[72:73], v[26:27], v[82:83] op_sel_hi:[0,1]
	v_med3_f32 v60, v60, s7, v57
	v_med3_f32 v61, v61, s7, v57
	v_cvt_pk_fp8_f32 v24, v60, v61 op_sel:[0,0,1]
	v_pk_mul_f32 v[70:71], v[26:27], v[84:85] op_sel_hi:[0,1]
	global_store_dword v[22:23], v24, off offset:256
	v_mov_b32_e32 v58, v130
	v_mov_b32_e32 v59, v131
	v_mov_b32_e32 v60, v132
	v_mov_b32_e32 v61, v133
	v_mov_b32_e32 v62, v134
	v_mov_b32_e32 v63, v135
	v_mov_b32_e32 v64, v136
	v_mov_b32_e32 v65, v137
	v_mov_b32_e32 v66, v138
	v_mov_b32_e32 v67, v139
	v_mov_b32_e32 v68, v140
	v_mov_b32_e32 v69, v141
	v_mov_b32_e32 v24, 0
	v_pk_mul_f32 v[58:59], v[58:59], v[72:73]
	v_pk_add_f32 v[62:63], v[62:63], 1.0 op_sel_hi:[1,0]
	v_pk_mul_f32 v[60:61], v[60:61], v[70:71]
	v_pk_fma_f32 v[58:59], v[58:59], v[62:63], v[66:67]
	v_pk_add_f32 v[64:65], v[64:65], 1.0 op_sel_hi:[1,0]
	v_med3_f32 v58, v58, s7, v57
	v_med3_f32 v59, v59, s7, v57
	v_cvt_pk_fp8_f32 v24, v58, v59
	v_pk_fma_f32 v[60:61], v[60:61], v[64:65], v[68:69]
	v_pk_mul_f32 v[72:73], v[88:89], v[26:27] op_sel_hi:[1,0]
	v_med3_f32 v60, v60, s7, v57
	v_med3_f32 v61, v61, s7, v57
	v_cvt_pk_fp8_f32 v24, v60, v61 op_sel:[0,0,1]
	v_pk_mul_f32 v[70:71], v[90:91], v[26:27] op_sel_hi:[1,0]
	global_store_dword v[22:23], v24, off offset:512
	v_mov_b32_e32 v58, v142
	v_mov_b32_e32 v59, v143
	v_mov_b32_e32 v60, v144
	v_mov_b32_e32 v61, v145
	v_mov_b32_e32 v62, v146
	v_mov_b32_e32 v63, v147
	v_mov_b32_e32 v64, v148
	v_mov_b32_e32 v65, v149
	v_mov_b32_e32 v66, v150
	v_mov_b32_e32 v67, v151
	v_mov_b32_e32 v68, v152
	v_mov_b32_e32 v69, v153
	v_mov_b32_e32 v24, 0
	v_pk_mul_f32 v[58:59], v[72:73], v[58:59]
	v_pk_add_f32 v[62:63], v[62:63], 1.0 op_sel_hi:[1,0]
	v_pk_mul_f32 v[60:61], v[70:71], v[60:61]
	v_pk_fma_f32 v[58:59], v[58:59], v[62:63], v[66:67]
	v_pk_add_f32 v[64:65], v[64:65], 1.0 op_sel_hi:[1,0]
	v_med3_f32 v58, v58, s7, v57
	v_med3_f32 v59, v59, s7, v57
	v_cvt_pk_fp8_f32 v24, v58, v59
	v_pk_fma_f32 v[60:61], v[60:61], v[64:65], v[68:69]
	v_mov_b32_e32 v70, v39
	v_med3_f32 v60, v60, s7, v57
	v_med3_f32 v61, v61, s7, v57
	v_cvt_pk_fp8_f32 v24, v60, v61 op_sel:[0,0,1]
	v_mov_b32_e32 v71, v41
	v_mov_b32_e32 v39, v40
	v_pk_mul_f32 v[40:41], v[26:27], v[70:71] op_sel_hi:[0,1]
	global_store_dword v[22:23], v24, off offset:768
	v_mov_b32_e32 v58, v154
	v_mov_b32_e32 v59, v155
	v_mov_b32_e32 v60, v156
	v_mov_b32_e32 v61, v157
	v_mov_b32_e32 v62, v158
	v_mov_b32_e32 v63, v159
	v_mov_b32_e32 v64, v160
	v_mov_b32_e32 v65, v161
	v_mov_b32_e32 v66, v162
	v_mov_b32_e32 v67, v163
	v_mov_b32_e32 v68, v164
	v_mov_b32_e32 v69, v165
	v_pk_mul_f32 v[38:39], v[26:27], v[38:39] op_sel_hi:[0,1]
	v_mov_b32_e32 v24, 0
	v_pk_mul_f32 v[38:39], v[38:39], v[58:59]
	v_pk_mul_f32 v[40:41], v[40:41], v[60:61]
	v_pk_add_f32 v[60:61], v[62:63], 1.0 op_sel_hi:[1,0]
	v_pk_add_f32 v[58:59], v[64:65], 1.0 op_sel_hi:[1,0]
	v_pk_fma_f32 v[38:39], v[38:39], v[60:61], v[66:67]
	v_pk_fma_f32 v[40:41], v[40:41], v[58:59], v[68:69]
	v_med3_f32 v38, v38, s7, v57
	v_med3_f32 v39, v39, s7, v57
	v_cvt_pk_fp8_f32 v24, v38, v39
	v_med3_f32 v40, v40, s7, v57
	v_med3_f32 v41, v41, s7, v57
	v_mov_b32_e32 v66, v35
	v_cvt_pk_fp8_f32 v24, v40, v41 op_sel:[0,0,1]
	v_mov_b32_e32 v67, v37
	v_mov_b32_e32 v35, v36
	v_pk_mul_f32 v[36:37], v[26:27], v[66:67] op_sel_hi:[0,1]
	global_store_dword v[22:23], v24, off offset:1024
	v_mov_b32_e32 v38, v166
	v_mov_b32_e32 v39, v167
	v_mov_b32_e32 v40, v168
	v_mov_b32_e32 v41, v169
	v_mov_b32_e32 v58, v170
	v_mov_b32_e32 v59, v171
	v_mov_b32_e32 v60, v172
	v_mov_b32_e32 v61, v173
	v_mov_b32_e32 v62, v174
	v_mov_b32_e32 v63, v175
	v_mov_b32_e32 v64, v176
	v_mov_b32_e32 v65, v177
	v_pk_mul_f32 v[34:35], v[26:27], v[34:35] op_sel_hi:[0,1]
	v_mov_b32_e32 v24, 0
	v_pk_mul_f32 v[34:35], v[34:35], v[38:39]
	v_pk_mul_f32 v[36:37], v[36:37], v[40:41]
	v_pk_add_f32 v[40:41], v[58:59], 1.0 op_sel_hi:[1,0]
	v_pk_add_f32 v[38:39], v[60:61], 1.0 op_sel_hi:[1,0]
	v_pk_fma_f32 v[34:35], v[34:35], v[40:41], v[62:63]
	v_pk_fma_f32 v[36:37], v[36:37], v[38:39], v[64:65]
	v_med3_f32 v34, v34, s7, v57
	v_med3_f32 v35, v35, s7, v57
	v_cvt_pk_fp8_f32 v24, v34, v35
	v_med3_f32 v36, v36, s7, v57
	v_med3_f32 v37, v37, s7, v57
	v_cvt_pk_fp8_f32 v24, v36, v37 op_sel:[0,0,1]
	global_store_dword v[22:23], v24, off offset:1280
	v_mov_b32_e32 v34, v182
	v_mov_b32_e32 v35, v183
	v_mov_b32_e32 v36, v184
	v_mov_b32_e32 v37, v185
	v_mov_b32_e32 v38, v186
	v_mov_b32_e32 v39, v187
	v_mov_b32_e32 v40, v188
	v_mov_b32_e32 v41, v189
	v_mov_b32_e32 v58, v190
	v_mov_b32_e32 v59, v191
	v_mov_b32_e32 v60, v192
	v_mov_b32_e32 v61, v193
	v_mov_b32_e32 v24, 0
	v_pk_mul_f32 v[30:31], v[30:31], v[34:35]
	v_pk_mul_f32 v[32:33], v[32:33], v[36:37]
	v_pk_add_f32 v[36:37], v[38:39], 1.0 op_sel_hi:[1,0]
	v_pk_add_f32 v[34:35], v[40:41], 1.0 op_sel_hi:[1,0]
	v_pk_fma_f32 v[30:31], v[30:31], v[36:37], v[58:59]
	v_pk_fma_f32 v[32:33], v[32:33], v[34:35], v[60:61]
	v_med3_f32 v30, v30, s7, v57
	v_med3_f32 v31, v31, s7, v57
	v_cvt_pk_fp8_f32 v24, v30, v31
	v_med3_f32 v32, v32, s7, v57
	v_med3_f32 v33, v33, s7, v57
	v_mov_b32_e32 v58, 0
	v_cvt_pk_fp8_f32 v24, v32, v33 op_sel:[0,0,1]
	global_store_dword v[22:23], v24, off offset:1536
	v_mov_b32_e32 v30, v194
	v_mov_b32_e32 v31, v195
	v_mov_b32_e32 v32, v196
	v_mov_b32_e32 v33, v197
	v_mov_b32_e32 v34, v198
	v_mov_b32_e32 v35, v199
	v_mov_b32_e32 v36, v200
	v_mov_b32_e32 v37, v201
	v_mov_b32_e32 v38, v202
	v_mov_b32_e32 v39, v203
	v_mov_b32_e32 v40, v204
	v_mov_b32_e32 v41, v205
	v_mov_b32_e32 v24, v27
	v_pk_mul_f32 v[24:25], v[24:25], v[26:27] op_sel_hi:[1,0]
	v_pk_mul_f32 v[26:27], v[28:29], v[32:33]
	v_pk_mul_f32 v[24:25], v[24:25], v[30:31]
	v_pk_add_f32 v[30:31], v[34:35], 1.0 op_sel_hi:[1,0]
	v_pk_add_f32 v[28:29], v[36:37], 1.0 op_sel_hi:[1,0]
	v_pk_fma_f32 v[24:25], v[24:25], v[30:31], v[38:39]
	s_nop 0
	v_med3_f32 v24, v24, s7, v57
	v_med3_f32 v25, v25, s7, v57
	v_cvt_pk_fp8_f32 v58, v24, v25
	v_pk_fma_f32 v[24:25], v[26:27], v[28:29], v[40:41]
	s_nop 0
	v_med3_f32 v24, v24, s7, v57
	v_med3_f32 v25, v25, s7, v57
	v_cvt_pk_fp8_f32 v58, v24, v25 op_sel:[0,0,1]
	global_store_dword v[22:23], v58, off offset:1792
	s_nop 1
	s_waitcnt vmcnt(8)
; #define GAS __attribute__((address_space(1)))
; template <bool F8, bool SRCH = false> __device__ __forceinline__ void norm_phase(Frame& F, const float* srcL, const float* srcC, const float* g, const float* mod, int shift_off, int scale_off, int nrows) {
;     ...
;         for (int j = 0; j < 8; ++j) {
;             if constexpr (SRCH) { const v2u w = ((const GAS v2u*)(WSP(const bf16, WS_H) + (size_t)row * DM))[F.lane + 64 * j]; v[j].x = bflo(w.x); v[j].y = bfhi(w.x); v[j].z = bflo(w.y); v[j].w = bfhi(w.y); }
;             else v[j] = xr[64 * j];
;             s += (v[j].x * v[j].x + v[j].y * v[j].y) + (v[j].z * v[j].z + v[j].w * v[j].w); }
	v_mov_b32_e32 v26, v206
	v_mov_b32_e32 v27, v207
	v_mov_b32_e32 v28, v208
	v_mov_b32_e32 v29, v209
	v_mov_b32_e32 v30, v210
	v_mov_b32_e32 v31, v211
	v_mov_b32_e32 v32, v212
	v_mov_b32_e32 v33, v213
	v_mov_b32_e32 v34, v214
	v_mov_b32_e32 v35, v215
	v_mov_b32_e32 v36, v216
	v_mov_b32_e32 v37, v217
	v_mov_b32_e32 v70, v218
	v_mov_b32_e32 v71, v219
	v_mov_b32_e32 v72, v220
	v_mov_b32_e32 v73, v221
	s_cbranch_scc1 .LBB0_603

; #define GAS __attribute__((address_space(1)))
; template <bool F8, bool SRCH = false> __device__ __forceinline__ void norm_phase(Frame& F, const float* srcL, const float* srcC, const float* g, const float* mod, int shift_off, int scale_off, int nrows) {
;     const int gw = F.vcu * NWAVES + F.wave, NGW = F.G * NWAVES;
;     bf16* XN = WSP(bf16, WS_XN);
;     for (int row = gw; row < nrows; row += NGW) {
;         const float* src = row < ML ? srcL + (size_t)row * DM : srcC + (size_t)(row - ML) * DM;
;         const float* mv = mod + (size_t)(row < ML ? (row >> 13) : 2) * MOD_W;
;         const GAS f32x4* xr = (const GAS f32x4*)src + F.lane;
;         f32x4 v[8]; float s = 0.f;
; #pragma unroll
;         for (int j = 0; j < 8; ++j) {
;             if constexpr (SRCH) { const v2u w = ((const GAS v2u*)(WSP(const bf16, WS_H) + (size_t)row * DM))[F.lane + 64 * j]; v[j].x = bflo(w.x); v[j].y = bfhi(w.x); v[j].z = bflo(w.y); v[j].w = bfhi(w.y); }
;             else v[j] = xr[64 * j];
;             s += (v[j].x * v[j].x + v[j].y * v[j].y) + (v[j].z * v[j].z + v[j].w * v[j].w); }
;         const float rstd = 1.0f / sqrtf(wave_sum(s) * (1.0f / DM) + NORM_EPS);
;         GAS v2u* o8 = (GAS v2u*)(XN + (size_t)row * DM) + F.lane;
; #pragma unroll
;         for (int j = 0; j < 8; ++j) { const int col = 4 * (F.lane + 64 * j);
;             const f32x4 gg = *(const GAS f32x4*)(g + col), sh = *(const GAS f32x4*)(mv + shift_off + col), sc = *(const GAS f32x4*)(mv + scale_off + col);
.LBB0_1064:
	s_cmp_lt_i32 s90, 10
	s_cselect_b64 s[0:1], -1, 0
	s_and_b64 s[2:3], s[0:1], s[4:5]
	s_andn2_b64 vcc, exec, s[2:3]
	s_cbranch_vccnz .LBB0_1068
	s_lshl_b32 s0, s92, 3
	s_add_i32 s4, s0, s94
	s_cmpk_gt_i32 s4, 0x41ff
	s_cbranch_scc1 .LBB0_1068
	v_mbcnt_lo_u32_b32 v1, -1, 0
	s_waitcnt vmcnt(0)
	v_mbcnt_hi_u32_b32 v2, -1, v1
	v_and_b32_e32 v1, 64, v2
	v_add_u32_e32 v3, 64, v1
	v_xor_b32_e32 v1, 1, v2
	v_cmp_lt_i32_e32 vcc, v1, v3
	v_xor_b32_e32 v4, 2, v2
	v_lshlrev_b32_e32 v14, 2, v178
	v_cndmask_b32_e32 v1, v2, v1, vcc
	v_cmp_lt_i32_e32 vcc, v4, v3
	s_add_u32 s14, s88, 0x124000
	v_mov_b32_e32 v13, 0
	v_cndmask_b32_e32 v4, v2, v4, vcc
	v_lshlrev_b32_e32 v28, 2, v4
	v_xor_b32_e32 v4, 4, v2
	v_cmp_lt_i32_e32 vcc, v4, v3
	v_lshlrev_b32_e32 v12, 4, v178
	v_or_b32_e32 v24, 0x500, v14
	v_cndmask_b32_e32 v4, v2, v4, vcc
	v_lshlrev_b32_e32 v29, 2, v4
	v_xor_b32_e32 v4, 8, v2
	v_cmp_lt_i32_e32 vcc, v4, v3
	s_addc_u32 s15, s89, 0
	s_mov_b64 s[0:1], 0x1000
	v_cndmask_b32_e32 v4, v2, v4, vcc
	v_lshlrev_b32_e32 v30, 2, v4
	v_xor_b32_e32 v4, 16, v2
	v_cmp_lt_i32_e32 vcc, v4, v3
	v_or_b32_e32 v26, 0x600, v14
	s_ashr_i32 s5, s4, 31
	v_cndmask_b32_e32 v4, v2, v4, vcc
	v_lshlrev_b32_e32 v31, 2, v4
	v_xor_b32_e32 v4, 32, v2
	v_cmp_lt_i32_e32 vcc, v4, v3
	s_lshl_b32 s6, s93, 3
	v_or_b32_e32 v42, 0x700, v14
	v_cndmask_b32_e32 v2, v2, v4, vcc
	v_lshlrev_b32_e32 v32, 2, v2
	v_lshl_add_u64 v[2:3], s[40:41], 0, v[12:13]
	v_lshlrev_b32_e32 v12, 2, v24
	v_lshl_add_u64 v[4:5], v[2:3], 0, s[0:1]
	v_lshl_add_u64 v[6:7], s[40:41], 0, v[12:13]
	v_lshlrev_b32_e32 v12, 2, v26
	s_lshl_b64 s[0:1], s[4:5], 12
	v_lshl_add_u64 v[8:9], s[40:41], 0, v[12:13]
	v_lshlrev_b32_e32 v12, 2, v42
	s_add_u32 s0, s88, s0
	v_lshl_add_u64 v[10:11], s[40:41], 0, v[12:13]
	v_lshlrev_b32_e32 v12, 3, v178
	s_addc_u32 s1, s89, s1
	v_or_b32_e32 v16, 0x100, v14
	v_or_b32_e32 v18, 0x200, v14
	v_or_b32_e32 v20, 0x300, v14
	v_or_b32_e32 v22, 0x400, v14
	v_lshl_add_u64 v[12:13], s[0:1], 0, v[12:13]
	s_mov_b64 s[0:1], 0x4d800000
	s_ashr_i32 s7, s6, 31
	v_lshlrev_b32_e32 v1, 2, v1
	v_lshl_add_u64 v[12:13], v[12:13], 0, s[0:1]
	s_lshl_b64 s[8:9], s[6:7], 12
	v_mov_b32_e32 v33, 0x358637bd
	s_mov_b32 s5, 0xf800000
	v_mov_b32_e32 v34, 0x260
	v_lshlrev_b32_e32 v35, 2, v14
	s_mov_b32 s7, 0xd0200000
	v_lshlrev_b32_e32 v36, 2, v16
	s_mov_b32 s16, 0xd0201000
	v_lshlrev_b32_e32 v37, 2, v18
	v_lshlrev_b32_e32 v38, 2, v20
	v_lshlrev_b32_e32 v39, 2, v22
	v_lshlrev_b32_e32 v40, 2, v24
	v_lshlrev_b32_e32 v41, 2, v26
	v_lshlrev_b32_e32 v42, 2, v42
	global_load_dwordx2 v[14:15], v[12:13], off
	global_load_dwordx2 v[16:17], v[12:13], off offset:512
	global_load_dwordx2 v[18:19], v[12:13], off offset:1024
	global_load_dwordx2 v[20:21], v[12:13], off offset:1536
	global_load_dwordx2 v[22:23], v[12:13], off offset:2048
	global_load_dwordx2 v[26:27], v[12:13], off offset:2560
	global_load_dwordx2 v[56:57], v[12:13], off offset:3072
	global_load_dwordx2 v[58:59], v[12:13], off offset:3584
.LBB0_1067:
	s_min_i32 s0, s4, 0x4000
	s_ashr_i32 s0, s0, 13
	s_mul_hi_i32 s1, s0, 0xc000
	s_mul_i32 s0, s0, 0xc000
	s_add_u32 s10, s14, s0
	s_addc_u32 s11, s15, s1
	s_add_u32 s12, s10, 0x2000
	s_addc_u32 s13, s11, 0
	global_load_dwordx4 v[44:47], v[2:3], off
	global_load_dwordx4 v[48:51], v35, s[10:11]
	global_load_dwordx4 v[52:55], v35, s[12:13]
	global_load_dwordx4 v[108:111], v[2:3], off offset:1024
	global_load_dwordx4 v[112:115], v36, s[12:13]
	global_load_dwordx4 v[116:119], v35, s[10:11] offset:1024
	global_load_dwordx4 v[120:123], v[2:3], off offset:2048
	global_load_dwordx4 v[124:127], v37, s[12:13]
	global_load_dwordx4 v[128:131], v35, s[10:11] offset:2048
	global_load_dwordx4 v[132:135], v[2:3], off offset:3072
	global_load_dwordx4 v[136:139], v38, s[12:13]
	global_load_dwordx4 v[140:143], v35, s[10:11] offset:3072
	global_load_dwordx4 v[144:147], v[4:5], off
	global_load_dwordx4 v[148:151], v39, s[12:13]
	global_load_dwordx4 v[152:155], v39, s[10:11]
	global_load_dwordx4 v[156:159], v[6:7], off
	global_load_dwordx4 v[160:163], v40, s[12:13]
	global_load_dwordx4 v[164:167], v40, s[10:11]
	global_load_dwordx4 v[168:171], v[8:9], off
	global_load_dwordx4 v[172:175], v41, s[12:13]
	global_load_dwordx4 v[182:185], v41, s[10:11]
	global_load_dwordx4 v[186:189], v[10:11], off
	global_load_dwordx4 v[190:193], v42, s[12:13]
	global_load_dwordx4 v[194:197], v42, s[10:11]
	v_add_co_u32_e32 v60, vcc, s7, v12
	s_add_i32 s4, s4, s6
	s_nop 0
	v_addc_co_u32_e32 v61, vcc, -1, v13, vcc
	s_cmpk_lt_i32 s4, 0x4200
	v_lshl_add_u64 v[214:215], v[12:13], 0, s[8:9]
	global_load_dwordx2 v[198:199], v[214:215], off
	global_load_dwordx2 v[200:201], v[214:215], off offset:512
	global_load_dwordx2 v[202:203], v[214:215], off offset:1024
	global_load_dwordx2 v[204:205], v[214:215], off offset:1536
	global_load_dwordx2 v[206:207], v[214:215], off offset:2048
	global_load_dwordx2 v[208:209], v[214:215], off offset:2560
	global_load_dwordx2 v[210:211], v[214:215], off offset:3072
	global_load_dwordx2 v[212:213], v[214:215], off offset:3584
	s_waitcnt vmcnt(32)
; #define GAS __attribute__((address_space(1)))
; __device__ __forceinline__ unsigned pk2(float lo, float hi) { return pg8::cvt_pk_bf16(lo, hi); }
; __device__ __forceinline__ unsigned pk4_fp8(float a, float b, float c, float d) { int p = 0; p = __builtin_amdgcn_cvt_pk_fp8_f32(a, b, p, false); p = __builtin_amdgcn_cvt_pk_fp8_f32(c, d, p, true); return (unsigned)p; }
; __device__ __forceinline__ float clamp8(float x) { return __builtin_fminf(__builtin_fmaxf(x, -448.0f), 448.0f); }
; template <bool F8, bool SRCH = false> __device__ __forceinline__ void norm_phase(Frame& F, const float* srcL, const float* srcC, const float* g, const float* mod, int shift_off, int scale_off, int nrows) {
;     ...
;             s += (v[j].x * v[j].x + v[j].y * v[j].y) + (v[j].z * v[j].z + v[j].w * v[j].w); }
;         const float rstd = 1.0f / sqrtf(wave_sum(s) * (1.0f / DM) + NORM_EPS);
;         GAS v2u* o8 = (GAS v2u*)(XN + (size_t)row * DM) + F.lane;
; #pragma unroll
;         for (int j = 0; j < 8; ++j) { const int col = 4 * (F.lane + 64 * j);
;             const f32x4 gg = *(const GAS f32x4*)(g + col), sh = *(const GAS f32x4*)(mv + shift_off + col), sc = *(const GAS f32x4*)(mv + scale_off + col);
;             const f32x4 y = v[j] * rstd * gg * (sc + 1.0f) + sh;
;             if (F8) { ((GAS unsigned*)((unsigned char*)XN + (size_t)row * DM))[F.lane + 64 * j] = pk4_fp8(clamp8(y.x), clamp8(y.y), clamp8(y.z), clamp8(y.w)); }
;             else { v2u w; w.x = pk2(y.x, y.y); w.y = pk2(y.z, y.w); o8[64 * j] = w; } }
	v_and_b32_e32 v63, 0xffff0000, v14
	v_and_b32_e32 v65, 0xffff0000, v15
	v_lshlrev_b32_e32 v62, 16, v14
	v_lshlrev_b32_e32 v64, 16, v15
	v_lshlrev_b32_e32 v67, 16, v17
	v_lshlrev_b32_e32 v66, 16, v16
	v_and_b32_e32 v69, 0xffff0000, v17
	v_and_b32_e32 v68, 0xffff0000, v16
	v_and_b32_e32 v71, 0xffff0000, v18
	v_and_b32_e32 v73, 0xffff0000, v19
	v_lshlrev_b32_e32 v75, 16, v20
	v_lshlrev_b32_e32 v17, 16, v58
	v_and_b32_e32 v15, 0xffff0000, v58
	v_mul_f32_e32 v14, v65, v65
	v_mul_f32_e32 v16, v63, v63
	v_lshlrev_b32_e32 v70, 16, v18
	v_lshlrev_b32_e32 v72, 16, v19
	v_and_b32_e32 v77, 0xffff0000, v20
	v_lshlrev_b32_e32 v78, 16, v21
	v_and_b32_e32 v79, 0xffff0000, v21
	v_lshlrev_b32_e32 v81, 16, v23
	v_lshlrev_b32_e32 v80, 16, v22
	v_and_b32_e32 v83, 0xffff0000, v23
	v_and_b32_e32 v82, 0xffff0000, v22
	v_lshlrev_b32_e32 v20, 16, v56
	v_and_b32_e32 v21, 0xffff0000, v56
	v_lshlrev_b32_e32 v22, 16, v57
	v_and_b32_e32 v23, 0xffff0000, v57
	v_lshlrev_b32_e32 v18, 16, v59
	v_and_b32_e32 v19, 0xffff0000, v59
	v_pk_mul_f32 v[56:57], v[68:69], v[68:69]
	v_mov_b32_e32 v59, v75
	v_mul_f32_e32 v58, v71, v71
	v_mul_f32_e32 v74, v73, v73
	v_pk_fma_f32 v[90:91], v[64:65], v[64:65], v[14:15] op_sel_hi:[1,1,0]
	v_pk_fma_f32 v[92:93], v[62:63], v[62:63], v[16:17] op_sel_hi:[1,1,0]
	v_pk_fma_f32 v[56:57], v[66:67], v[66:67], v[56:57]
	v_pk_fma_f32 v[94:95], v[70:71], v[70:71], v[58:59] op_sel_hi:[1,1,0]
	v_pk_fma_f32 v[96:97], v[72:73], v[72:73], v[74:75] op_sel_hi:[1,1,0]
	v_mov_b32_e32 v74, v92
	v_mov_b32_e32 v58, v90
	v_mul_f32_e32 v43, v77, v77
	v_mul_f32_e32 v102, v78, v78
	v_mul_f32_e32 v103, v79, v79
	v_pk_add_f32 v[90:91], v[92:93], v[90:91]
	v_pk_add_f32 v[56:57], v[56:57], v[56:57] op_sel:[0,1] op_sel_hi:[1,0]
	v_pk_mul_f32 v[58:59], v[74:75], v[58:59]
	v_mov_b32_e32 v95, v102
	v_mov_b32_e32 v97, v103
	v_mov_b32_e32 v57, v43
	v_mov_b32_e32 v91, v59
	v_pk_mul_f32 v[84:85], v[82:83], v[82:83]
	v_pk_add_f32 v[92:93], v[94:95], v[96:97]
	v_pk_add_f32 v[56:57], v[90:91], v[56:57]
	v_lshlrev_b32_e32 v25, 16, v27
	v_lshlrev_b32_e32 v24, 16, v26
	v_and_b32_e32 v27, 0xffff0000, v27
	v_and_b32_e32 v26, 0xffff0000, v26
	v_pk_fma_f32 v[84:85], v[80:81], v[80:81], v[84:85]
	v_pk_add_f32 v[56:57], v[56:57], v[92:93]
	v_pk_mul_f32 v[86:87], v[26:27], v[26:27]
	v_mov_b32_e32 v89, v17
	v_mul_f32_e32 v88, v23, v23
	v_pk_add_f32 v[84:85], v[84:85], v[84:85] op_sel:[0,1] op_sel_hi:[1,0]
	v_pk_add_f32 v[56:57], v[56:57], v[56:57] op_sel:[0,1] op_sel_hi:[1,0]
	v_mul_f32_e32 v76, v21, v21
	v_pk_fma_f32 v[86:87], v[24:25], v[24:25], v[86:87]
	v_pk_fma_f32 v[100:101], v[22:23], v[22:23], v[88:89] op_sel_hi:[1,1,0]
	v_mov_b32_e32 v88, v84
	v_mov_b32_e32 v16, v56
	v_mul_f32_e32 v104, v15, v15
	v_mul_f32_e32 v105, v18, v18
	v_mul_f32_e32 v106, v19, v19
	v_pk_fma_f32 v[98:99], v[20:21], v[20:21], v[76:77] op_sel_hi:[1,1,0]
	v_pk_add_f32 v[86:87], v[86:87], v[86:87] op_sel:[0,1] op_sel_hi:[1,0]
	v_pk_add_f32 v[56:57], v[56:57], v[84:85]
	v_pk_mul_f32 v[58:59], v[16:17], v[88:89]
	v_mov_b32_e32 v99, v105
	v_mov_b32_e32 v101, v106
	v_mov_b32_e32 v87, v104
	v_mov_b32_e32 v57, v59
	v_pk_add_f32 v[94:95], v[98:99], v[100:101]
	v_pk_add_f32 v[56:57], v[56:57], v[86:87]
	s_waitcnt vmcnt(8)
	v_pk_add_f32 v[52:53], v[52:53], 1.0 op_sel_hi:[1,0]
	v_pk_add_f32 v[56:57], v[56:57], v[94:95]
	v_pk_add_f32 v[54:55], v[54:55], 1.0 op_sel_hi:[1,0]
	v_add_f32_e32 v14, v56, v57
	ds_bpermute_b32 v16, v1, v14
	v_mov_b32_e32 v76, v75
	s_waitcnt lgkmcnt(0)
	v_add_f32_e32 v14, v14, v16
	ds_bpermute_b32 v16, v28, v14
	s_waitcnt lgkmcnt(0)
	v_add_f32_e32 v14, v14, v16
	ds_bpermute_b32 v16, v29, v14
	s_waitcnt lgkmcnt(0)
	v_add_f32_e32 v14, v14, v16
	ds_bpermute_b32 v16, v30, v14
	s_waitcnt lgkmcnt(0)
	v_add_f32_e32 v14, v14, v16
	ds_bpermute_b32 v16, v31, v14
	s_waitcnt lgkmcnt(0)
	v_add_f32_e32 v14, v14, v16
	ds_bpermute_b32 v16, v32, v14
	s_waitcnt lgkmcnt(0)
	v_add_f32_e32 v14, v14, v16
	v_fmamk_f32 v14, v14, 0x3a000000, v33
	v_mul_f32_e32 v16, 0x4f800000, v14
	v_cmp_gt_f32_e32 vcc, s5, v14
	s_nop 1
	v_cndmask_b32_e32 v14, v14, v16, vcc
	v_sqrt_f32_e32 v16, v14
	s_nop 0
	v_add_u32_e32 v43, -1, v16
	v_add_u32_e32 v56, 1, v16
	v_fma_f32 v57, -v43, v16, v14
	v_fma_f32 v58, -v56, v16, v14
	v_cmp_ge_f32_e64 s[0:1], 0, v57
	s_nop 1
	v_cndmask_b32_e64 v16, v16, v43, s[0:1]
	v_cmp_lt_f32_e64 s[0:1], 0, v58
	s_nop 1
	v_cndmask_b32_e64 v16, v16, v56, s[0:1]
	v_mul_f32_e32 v43, 0x37800000, v16
	v_cndmask_b32_e32 v16, v16, v43, vcc
	v_cmp_class_f32_e32 vcc, v14, v34
	s_nop 1
	v_cndmask_b32_e32 v14, v16, v14, vcc
	v_div_scale_f32 v16, s[0:1], v14, v14, 1.0
	v_rcp_f32_e32 v56, v16
	v_div_scale_f32 v43, vcc, 1.0, v14, 1.0
	v_fma_f32 v57, -v16, v56, 1.0
	v_fmac_f32_e32 v56, v57, v56
	v_mul_f32_e32 v57, v43, v56
	v_fma_f32 v58, -v16, v57, v43
	v_fmac_f32_e32 v57, v58, v56
	v_fma_f32 v16, -v16, v57, v43
	v_div_fmas_f32 v16, v16, v56, v57
	v_div_fixup_f32 v16, v16, v14, 1.0
	v_pk_mul_f32 v[58:59], v[16:17], v[62:63] op_sel_hi:[0,1]
	v_pk_mul_f32 v[56:57], v[16:17], v[64:65] op_sel_hi:[0,1]
	v_pk_mul_f32 v[44:45], v[44:45], v[58:59]
	v_pk_mul_f32 v[46:47], v[46:47], v[56:57]
	v_pk_fma_f32 v[44:45], v[52:53], v[44:45], v[48:49]
	v_pk_fma_f32 v[46:47], v[54:55], v[46:47], v[50:51]
	v_cvt_pk_bf16_f32 v44, v44, v45
	v_mov_b32_e32 v58, v67
	v_cvt_pk_bf16_f32 v45, v46, v47
	global_store_dwordx2 v[60:61], v[44:45], off
	v_mov_b32_e32 v44, v108
	v_mov_b32_e32 v45, v109
	v_mov_b32_e32 v46, v110
	v_mov_b32_e32 v47, v111
	s_nop 0
	v_mov_b32_e32 v48, v112
	v_mov_b32_e32 v49, v113
	v_mov_b32_e32 v50, v114
	v_mov_b32_e32 v51, v115
	v_mov_b32_e32 v52, v116
	v_mov_b32_e32 v53, v117
	v_mov_b32_e32 v54, v118
	v_mov_b32_e32 v55, v119
; #define GAS __attribute__((address_space(1)))
; __device__ __forceinline__ unsigned pk2(float lo, float hi) { return pg8::cvt_pk_bf16(lo, hi); }
; __device__ __forceinline__ unsigned pk4_fp8(float a, float b, float c, float d) { int p = 0; p = __builtin_amdgcn_cvt_pk_fp8_f32(a, b, p, false); p = __builtin_amdgcn_cvt_pk_fp8_f32(c, d, p, true); return (unsigned)p; }
; __device__ __forceinline__ float clamp8(float x) { return __builtin_fminf(__builtin_fmaxf(x, -448.0f), 448.0f); }
; template <bool F8, bool SRCH = false> __device__ __forceinline__ void norm_phase(Frame& F, const float* srcL, const float* srcC, const float* g, const float* mod, int shift_off, int scale_off, int nrows) {
;     ...
;             if constexpr (SRCH) { const v2u w = ((const GAS v2u*)(WSP(const bf16, WS_H) + (size_t)row * DM))[F.lane + 64 * j]; v[j].x = bflo(w.x); v[j].y = bfhi(w.x); v[j].z = bflo(w.y); v[j].w = bfhi(w.y); }
;     ...
;         for (int j = 0; j < 8; ++j) { const int col = 4 * (F.lane + 64 * j);
;             const f32x4 gg = *(const GAS f32x4*)(g + col), sh = *(const GAS f32x4*)(mv + shift_off + col), sc = *(const GAS f32x4*)(mv + scale_off + col);
;             const f32x4 y = v[j] * rstd * gg * (sc + 1.0f) + sh;
;             if (F8) { ((GAS unsigned*)((unsigned char*)XN + (size_t)row * DM))[F.lane + 64 * j] = pk4_fp8(clamp8(y.x), clamp8(y.y), clamp8(y.z), clamp8(y.w)); }
;             else { v2u w; w.x = pk2(y.x, y.y); w.y = pk2(y.z, y.w); o8[64 * j] = w; } }
	v_mov_b32_e32 v67, v68
	v_mov_b32_e32 v59, v69
	v_pk_mul_f32 v[60:61], v[16:17], v[66:67] op_sel_hi:[0,1]
	v_add_co_u32_e32 v56, vcc, s16, v12
	v_pk_mul_f32 v[58:59], v[16:17], v[58:59] op_sel_hi:[0,1]
	s_nop 0
	v_addc_co_u32_e32 v57, vcc, -1, v13, vcc
	v_pk_mul_f32 v[22:23], v[16:17], v[22:23] op_sel_hi:[0,1]
	v_pk_mul_f32 v[20:21], v[16:17], v[20:21] op_sel_hi:[0,1]
	v_mov_b32_e32 v14, v17
	v_pk_mul_f32 v[14:15], v[14:15], v[16:17] op_sel_hi:[1,0]
	v_pk_mul_f32 v[18:19], v[18:19], v[16:17] op_sel_hi:[1,0]
	v_lshl_add_u64 v[12:13], v[12:13], 0, s[8:9]
	v_pk_mul_f32 v[44:45], v[44:45], v[60:61]
	v_pk_add_f32 v[48:49], v[48:49], 1.0 op_sel_hi:[1,0]
	v_pk_mul_f32 v[46:47], v[46:47], v[58:59]
	v_pk_add_f32 v[50:51], v[50:51], 1.0 op_sel_hi:[1,0]
	v_pk_fma_f32 v[44:45], v[48:49], v[44:45], v[52:53]
	v_pk_fma_f32 v[46:47], v[50:51], v[46:47], v[54:55]
	v_cvt_pk_bf16_f32 v44, v44, v45
	v_pk_mul_f32 v[60:61], v[16:17], v[70:71] op_sel_hi:[0,1]
	v_cvt_pk_bf16_f32 v45, v46, v47
	global_store_dwordx2 v[56:57], v[44:45], off offset:-3584
	v_mov_b32_e32 v44, v120
	v_mov_b32_e32 v45, v121
	v_mov_b32_e32 v46, v122
	v_mov_b32_e32 v47, v123
	s_nop 0
	v_mov_b32_e32 v48, v124
	v_mov_b32_e32 v49, v125
	v_mov_b32_e32 v50, v126
	v_mov_b32_e32 v51, v127
	v_mov_b32_e32 v52, v128
	v_mov_b32_e32 v53, v129
	v_mov_b32_e32 v54, v130
	v_mov_b32_e32 v55, v131
	v_pk_mul_f32 v[58:59], v[16:17], v[72:73] op_sel_hi:[0,1]
	v_pk_mul_f32 v[44:45], v[44:45], v[60:61]
	v_pk_add_f32 v[48:49], v[48:49], 1.0 op_sel_hi:[1,0]
	v_pk_mul_f32 v[46:47], v[46:47], v[58:59]
	v_pk_add_f32 v[50:51], v[50:51], 1.0 op_sel_hi:[1,0]
	v_pk_fma_f32 v[44:45], v[44:45], v[48:49], v[52:53]
	v_pk_fma_f32 v[46:47], v[46:47], v[50:51], v[54:55]
	v_cvt_pk_bf16_f32 v44, v44, v45
	v_pk_mul_f32 v[60:61], v[76:77], v[16:17] op_sel_hi:[1,0]
	v_cvt_pk_bf16_f32 v45, v46, v47
	global_store_dwordx2 v[56:57], v[44:45], off offset:-3072
	v_mov_b32_e32 v44, v132
	v_mov_b32_e32 v45, v133
	v_mov_b32_e32 v46, v134
	v_mov_b32_e32 v47, v135
	s_nop 0
	v_mov_b32_e32 v48, v136
	v_mov_b32_e32 v49, v137
	v_mov_b32_e32 v50, v138
	v_mov_b32_e32 v51, v139
	v_mov_b32_e32 v52, v140
	v_mov_b32_e32 v53, v141
	v_mov_b32_e32 v54, v142
	v_mov_b32_e32 v55, v143
	v_pk_mul_f32 v[58:59], v[78:79], v[16:17] op_sel_hi:[1,0]
	v_pk_mul_f32 v[44:45], v[60:61], v[44:45]
	v_pk_add_f32 v[48:49], v[48:49], 1.0 op_sel_hi:[1,0]
	v_pk_mul_f32 v[46:47], v[58:59], v[46:47]
	v_pk_add_f32 v[50:51], v[50:51], 1.0 op_sel_hi:[1,0]
	v_pk_fma_f32 v[44:45], v[44:45], v[48:49], v[52:53]
	v_pk_fma_f32 v[46:47], v[46:47], v[50:51], v[54:55]
	v_cvt_pk_bf16_f32 v44, v44, v45
	v_mov_b32_e32 v58, v81
	v_cvt_pk_bf16_f32 v45, v46, v47
	global_store_dwordx2 v[56:57], v[44:45], off offset:-2560
	v_mov_b32_e32 v44, v144
	v_mov_b32_e32 v45, v145
	v_mov_b32_e32 v46, v146
	v_mov_b32_e32 v47, v147
	s_nop 0
	v_mov_b32_e32 v48, v148
	v_mov_b32_e32 v49, v149
	v_mov_b32_e32 v50, v150
	v_mov_b32_e32 v51, v151
	v_mov_b32_e32 v52, v152
	v_mov_b32_e32 v53, v153
	v_mov_b32_e32 v54, v154
	v_mov_b32_e32 v55, v155
	v_mov_b32_e32 v81, v82
	v_mov_b32_e32 v59, v83
	v_pk_mul_f32 v[60:61], v[16:17], v[80:81] op_sel_hi:[0,1]
	v_pk_mul_f32 v[58:59], v[16:17], v[58:59] op_sel_hi:[0,1]
	v_pk_mul_f32 v[44:45], v[60:61], v[44:45]
	v_pk_add_f32 v[48:49], v[48:49], 1.0 op_sel_hi:[1,0]
	v_pk_mul_f32 v[46:47], v[58:59], v[46:47]
	v_pk_add_f32 v[50:51], v[50:51], 1.0 op_sel_hi:[1,0]
	v_pk_fma_f32 v[44:45], v[44:45], v[48:49], v[52:53]
	v_pk_fma_f32 v[46:47], v[46:47], v[50:51], v[54:55]
	v_cvt_pk_bf16_f32 v44, v44, v45
	v_mov_b32_e32 v58, v25
	v_cvt_pk_bf16_f32 v45, v46, v47
	global_store_dwordx2 v[56:57], v[44:45], off offset:-2048
	v_mov_b32_e32 v44, v156
	v_mov_b32_e32 v45, v157
	v_mov_b32_e32 v46, v158
	v_mov_b32_e32 v47, v159
	s_nop 0
	v_mov_b32_e32 v48, v160
	v_mov_b32_e32 v49, v161
	v_mov_b32_e32 v50, v162
	v_mov_b32_e32 v51, v163
	v_mov_b32_e32 v52, v164
	v_mov_b32_e32 v53, v165
	v_mov_b32_e32 v54, v166
	v_mov_b32_e32 v55, v167
	v_mov_b32_e32 v59, v27
	v_mov_b32_e32 v25, v26
	v_pk_mul_f32 v[26:27], v[16:17], v[58:59] op_sel_hi:[0,1]
	v_pk_mul_f32 v[24:25], v[16:17], v[24:25] op_sel_hi:[0,1]
	v_pk_mul_f32 v[24:25], v[24:25], v[44:45]
	v_pk_mul_f32 v[26:27], v[26:27], v[46:47]
	v_pk_add_f32 v[46:47], v[48:49], 1.0 op_sel_hi:[1,0]
	v_pk_add_f32 v[44:45], v[50:51], 1.0 op_sel_hi:[1,0]
	v_pk_fma_f32 v[24:25], v[24:25], v[46:47], v[52:53]
	v_pk_fma_f32 v[26:27], v[26:27], v[44:45], v[54:55]
	v_cvt_pk_bf16_f32 v24, v24, v25
	s_nop 0
	v_cvt_pk_bf16_f32 v25, v26, v27
	global_store_dwordx2 v[56:57], v[24:25], off offset:-1536
	v_mov_b32_e32 v24, v168
	v_mov_b32_e32 v25, v169
	v_mov_b32_e32 v26, v170
	v_mov_b32_e32 v27, v171
	s_nop 0
	v_mov_b32_e32 v44, v172
	v_mov_b32_e32 v45, v173
	v_mov_b32_e32 v46, v174
	v_mov_b32_e32 v47, v175
	v_mov_b32_e32 v48, v182
	v_mov_b32_e32 v49, v183
	v_mov_b32_e32 v50, v184
	v_mov_b32_e32 v51, v185
	v_pk_mul_f32 v[20:21], v[20:21], v[24:25]
	v_pk_mul_f32 v[22:23], v[22:23], v[26:27]
	v_pk_add_f32 v[26:27], v[44:45], 1.0 op_sel_hi:[1,0]
	v_pk_add_f32 v[24:25], v[46:47], 1.0 op_sel_hi:[1,0]
	v_pk_fma_f32 v[20:21], v[20:21], v[26:27], v[48:49]
	v_pk_fma_f32 v[22:23], v[22:23], v[24:25], v[50:51]
	v_cvt_pk_bf16_f32 v20, v20, v21
	s_nop 0
	v_cvt_pk_bf16_f32 v21, v22, v23
	global_store_dwordx2 v[56:57], v[20:21], off offset:-1024
	v_mov_b32_e32 v20, v186
	v_mov_b32_e32 v21, v187
	v_mov_b32_e32 v22, v188
	v_mov_b32_e32 v23, v189
	s_nop 0
	v_mov_b32_e32 v24, v190
	v_mov_b32_e32 v25, v191
	v_mov_b32_e32 v26, v192
	v_mov_b32_e32 v27, v193
	v_mov_b32_e32 v44, v194
	v_mov_b32_e32 v45, v195
	v_mov_b32_e32 v46, v196
	v_mov_b32_e32 v47, v197
	v_pk_mul_f32 v[14:15], v[14:15], v[20:21]
	v_pk_add_f32 v[20:21], v[24:25], 1.0 op_sel_hi:[1,0]
	v_pk_mul_f32 v[16:17], v[18:19], v[22:23]
	v_pk_add_f32 v[18:19], v[26:27], 1.0 op_sel_hi:[1,0]
	v_pk_fma_f32 v[14:15], v[14:15], v[20:21], v[44:45]
	v_pk_fma_f32 v[16:17], v[16:17], v[18:19], v[46:47]
	v_cvt_pk_bf16_f32 v14, v14, v15
	s_nop 0
	v_cvt_pk_bf16_f32 v15, v16, v17
	global_store_dwordx2 v[56:57], v[14:15], off offset:-512
	s_nop 1
	s_waitcnt vmcnt(8)
	v_mov_b32_e32 v14, v198
	v_mov_b32_e32 v15, v199
	v_mov_b32_e32 v16, v200
	v_mov_b32_e32 v17, v201
	v_mov_b32_e32 v18, v202
	v_mov_b32_e32 v19, v203
	v_mov_b32_e32 v20, v204
	v_mov_b32_e32 v21, v205
	v_mov_b32_e32 v22, v206
	v_mov_b32_e32 v23, v207
	v_mov_b32_e32 v26, v208
	v_mov_b32_e32 v27, v209
	v_mov_b32_e32 v56, v210
	v_mov_b32_e32 v57, v211
	v_mov_b32_e32 v58, v212
	v_mov_b32_e32 v59, v213
	s_cbranch_scc1 .LBB0_1067
